# attention steps: K reads first; the step's LDS-DMA requests issue in the wait-state slot behind the QK MFMAs
# speedup vs baseline: 1.0151x; 1.0016x over previous
; #define ATT_DMA(t, slot) do { glds16(ksrc + (long)(t) * tstep, (unsigned)__builtin_amdgcn_readfirstlane(kdst + (slot))); glds16(vsrc + (long)(t) * tstep, (unsigned)__builtin_amdgcn_readfirstlane(vdst + (slot))); } while (0)
; template <class BIAS>
; __device__ __forceinline__ void attn_tiles(char* shm, const UnitIO& io, int t_begin, int t_end, const BIAS& B, int tid) {
;     ...
;         if (rem > 3) ATT_DMA(t + 3, ((t + 3 - t_begin) & 3) * SLOTB);
;     ...
;             for (int d0 = 0; d0 < 4; ++d0) { c0 = __builtin_amdgcn_mfma_f32_32x32x16_bf16(kf[2 * d0], qr[d0], c0, 0, 0, 0); c1 = __builtin_amdgcn_mfma_f32_32x32x16_bf16(kf[2 * d0 + 1], qr[d0], c1, 0, 0, 0); }
;             float s0 = 0.f;
; #pragma unroll
;             for (int r = 0; r < 16; ++r) c0[r] = __builtin_amdgcn_exp2f(c0[r]);
;             { f32x2_t s2 = (f32x2_t){c0[0], c0[1]};
; #pragma unroll
;               for (int i = 1; i < 8; ++i) s2 += (f32x2_t){c0[2 * i], c0[2 * i + 1]};
;               s0 = s2[0] + s2[1]; }
.LBB0_303:
	s_waitcnt lgkmcnt(0)
	s_nop 0
	v_mfma_f32_32x32x16_bf16 v[50:65], v[98:101], v[66:69], v[50:65]
	v_mfma_f32_32x32x16_bf16 v[50:65], v[102:105], v[70:73], v[50:65]
	v_mfma_f32_32x32x16_bf16 v[50:65], v[106:109], v[74:77], v[50:65]
	v_mfma_f32_32x32x16_bf16 v[50:65], v[110:113], v[78:81], v[50:65]
	v_mfma_f32_32x32x16_bf16 v[34:49], v[94:97], v[66:69], v[34:49]
	s_and_b64 vcc, exec, s[12:13]
	s_cbranch_vccnz .Lmo_nodmaA
	s_and_b32 s100, s22, 0x6000
	s_add_i32 s101, s100, s29
	s_mov_b32 m0, s101
	s_add_i32 s100, s100, s33
	global_load_lds_dwordx4 v[172:173], off
	s_mov_b32 m0, s100
	s_nop 0
	global_load_lds_dwordx4 v[152:153], off
	s_nop 1
	s_branch .Lmo_go
.Lmo_nodmaA:
	s_nop 10
.Lmo_go:
	v_exp_f32_e32 v50, v50
	v_exp_f32_e32 v51, v51
	v_exp_f32_e32 v52, v52
	v_exp_f32_e32 v53, v53
	v_mfma_f32_32x32x16_bf16 v[34:49], v[90:93], v[70:73], v[34:49]
	v_exp_f32_e32 v98, v54
	v_exp_f32_e32 v99, v55
	v_exp_f32_e32 v100, v56
	v_exp_f32_e32 v101, v57
	v_mfma_f32_32x32x16_bf16 v[34:49], v[86:89], v[74:77], v[34:49]
	v_exp_f32_e32 v54, v58
	v_exp_f32_e32 v55, v59
	v_exp_f32_e32 v56, v60
	v_exp_f32_e32 v57, v61
	v_mfma_f32_32x32x16_bf16 v[34:49], v[82:85], v[78:81], v[34:49]
	v_exp_f32_e32 v58, v62
	v_exp_f32_e32 v59, v63
	v_add_f32_e32 v62, v50, v52
	v_add_f32_e32 v63, v51, v53
	v_add_f32_e64 v62, v98, v62
	v_add_f32_e64 v63, v99, v63
	v_exp_f32_e32 v60, v64
	v_exp_f32_e32 v61, v65
	v_add_f32_e32 v62, v100, v62
	v_add_f32_e32 v63, v101, v63
	v_cvt_pk_bf16_f32 v50, v50, v51
	v_add_f32_e32 v62, v54, v62
	v_add_f32_e32 v63, v55, v63
	v_cvt_pk_bf16_f32 v54, v54, v55
	v_add_f32_e32 v62, v56, v62
	v_add_f32_e32 v63, v57, v63
	v_cvt_pk_bf16_f32 v51, v52, v53
	v_add_f32_e32 v62, v58, v62
	v_add_f32_e32 v63, v59, v63
	v_cvt_pk_bf16_f32 v55, v56, v57
	v_add_f32_e32 v62, v60, v62
	v_add_f32_e32 v63, v61, v63
	v_cvt_pk_bf16_f32 v52, v98, v99
	v_add_f32_e32 v62, v62, v63
	v_cvt_pk_bf16_f32 v56, v58, v59
	v_cvt_pk_bf16_f32 v53, v100, v101
	v_cvt_pk_bf16_f32 v57, v60, v61
	v_add_f32_e32 v139, v139, v62
	s_and_b64 vcc, exec, s[4:5]
	s_cbranch_vccz .LBB0_311

;     __device__ __forceinline__ void init(f32x16& c0, f32x16& c1, int t) const {
;         const lds_fptr p = cs2 + 64 * t + 4 * hi;
;         f32x4 a[4], b[4];
; #pragma unroll
;         for (int g = 0; g < 4; ++g) { a[g] = *(const __attribute__((address_space(3))) f32x4*)(p + 8 * g); b[g] = *(const __attribute__((address_space(3))) f32x4*)(p + 32 + 8 * g); }
;         asm volatile("" : "+v"(a[0]), "+v"(a[1]), "+v"(a[2]), "+v"(a[3]), "+v"(b[0]), "+v"(b[1]), "+v"(b[2]), "+v"(b[3]));
; #pragma unroll
;         for (int g = 0; g < 4; ++g) { const f32x2_t a0 = (f32x2_t){a[g][0], a[g][1]}, a1 = (f32x2_t){a[g][2], a[g][3]}, b0 = (f32x2_t){b[g][0], b[g][1]}, b1 = (f32x2_t){b[g][2], b[g][3]};
;             const f32x2_t x0 = base - a0, x1 = base - a1, y0 = base - b0, y1 = base - b1;
;             c0[4 * g] = x0[0]; c0[4 * g + 1] = x0[1]; c0[4 * g + 2] = x1[0]; c0[4 * g + 3] = x1[1]; c1[4 * g] = y0[0]; c1[4 * g + 1] = y0[1]; c1[4 * g + 2] = y1[0]; c1[4 * g + 3] = y1[1]; }
;         if (t - nb0 == (w >> 1)) {
; #pragma unroll
;             for (int r = 0; r < 16; ++r) { const int ko = (r & 3) + 8 * (r >> 2); if (ko > u) c0[r] = ATT_NEG; if (ko > u - 32) c1[r] = ATT_NEG; }
;         }
; template <class BIAS>
; __device__ __forceinline__ void attn_tiles(char* shm, const UnitIO& io, int t_begin, int t_end, const BIAS& B, int tid) {
;     ...
;         const int rem = t_end - t;
;         const bool act = B.active(t);
;         const int sl_c = ((t - t_begin) & 3) * SLOTB;
;         if (rem > 3) ATT_DMA(t + 3, ((t + 3 - t_begin) & 3) * SLOTB);
;         u32x4 pw[4]; f32x16 c1x;
;         if (act) {
;             bf16x8 kf[8]; const lds_cptr kp = kp0 + sl_c;
; #pragma unroll
;             for (int j = 0; j < 4; ++j) { kf[2 * j] = *(const __attribute__((address_space(3))) bf16x8*)(kp + j * 2048); kf[2 * j + 1] = *(const __attribute__((address_space(3))) bf16x8*)(kp + j * 2048 + 512); }
;             ATT_SBAR();
;             f32x16 c0, c1; B.init(c0, c1, t);
;             ATT_SBAR();
;             asm volatile("" : "+v"(kf[0]), "+v"(kf[1]), "+v"(kf[2]), "+v"(kf[3]), "+v"(kf[4]), "+v"(kf[5]), "+v"(kf[6]), "+v"(kf[7]));
; #pragma unroll
;             for (int d0 = 0; d0 < 4; ++d0) { c0 = __builtin_amdgcn_mfma_f32_32x32x16_bf16(kf[2 * d0], qr[d0], c0, 0, 0, 0); c1 = __builtin_amdgcn_mfma_f32_32x32x16_bf16(kf[2 * d0 + 1], qr[d0], c1, 0, 0, 0); }
.LBB0_341:
.LBB0_342:
	s_add_i32 s20, s44, -3
	s_add_i32 s45, s37, s44
	s_cmp_lt_i32 s20, s51
	s_cselect_b64 s[20:21], -1, 0
	s_add_i32 s22, s45, -3
	s_cmp_le_i32 s22, s73
	s_cselect_b64 s[34:35], -1, 0
	s_or_b64 vcc, s[20:21], s[34:35]
	s_add_i32 s20, s39, 0xffffa000
	v_cndmask_b32_e64 v74, 0, 1, vcc
	s_and_b32 s20, s20, 0x6000
	v_cmp_ne_u32_e64 s[34:35], 1, v74
	s_andn2_b64 vcc, exec, vcc
	s_cbranch_vccnz .Lfx_inact
	v_add_u32_e32 v50, s20, v181
	ds_read_b128 v[114:117], v50
	ds_read_b128 v[110:113], v50 offset:512
	ds_read_b128 v[118:121], v50 offset:2048
	ds_read_b128 v[106:109], v50 offset:2560
	ds_read_b128 v[122:125], v50 offset:4096
	ds_read_b128 v[102:105], v50 offset:4608
	ds_read_b128 v[126:129], v50 offset:6144
	ds_read_b128 v[98:101], v50 offset:6656
	s_add_i32 s21, s36, s44
	ds_read_b128 v[50:53], v137 offset:224
	ds_read_b128 v[54:57], v137 offset:192
	ds_read_b128 v[58:61], v137 offset:96
	ds_read_b128 v[62:65], v137 offset:64
	ds_read_b128 v[218:221], v137 offset:160
	ds_read_b128 v[234:237], v137 offset:128
	ds_read_b128 v[66:69], v137
	ds_read_b128 v[70:73], v137 offset:32
	s_cmp_lg_u32 s21, 3
	s_waitcnt lgkmcnt(0)
	s_nop 0
	v_sub_f32_e32 v81, v33, v61
	v_sub_f32_e32 v80, v32, v60
	v_sub_f32_e32 v79, v31, v59
	v_sub_f32_e32 v78, v30, v58
	v_sub_f32_e32 v77, v29, v65
	v_sub_f32_e32 v76, v28, v64
	v_sub_f32_e32 v75, v11, v63
	v_sub_f32_e32 v74, v10, v62
	v_sub_f32_e32 v73, v9, v73
	v_sub_f32_e32 v72, v8, v72
	v_sub_f32_e32 v71, v7, v71
	v_sub_f32_e32 v70, v6, v70
	v_sub_f32_e32 v69, v5, v69
	v_sub_f32_e32 v68, v4, v68
	v_sub_f32_e32 v67, v3, v67
	v_sub_f32_e32 v66, v2, v66
	v_sub_f32_e32 v65, v33, v53
	v_sub_f32_e32 v64, v32, v52
	v_sub_f32_e32 v63, v31, v51
	v_sub_f32_e32 v62, v30, v50
	v_sub_f32_e32 v61, v29, v57
	v_sub_f32_e32 v60, v28, v56
	v_sub_f32_e32 v59, v11, v55
	v_sub_f32_e32 v58, v10, v54
	v_sub_f32_e32 v57, v9, v221
	v_sub_f32_e32 v56, v8, v220
	v_sub_f32_e32 v55, v7, v219
	v_sub_f32_e32 v54, v6, v218
	v_sub_f32_e32 v53, v5, v237
	v_sub_f32_e32 v52, v4, v236
	v_sub_f32_e32 v51, v3, v235
	v_sub_f32_e32 v50, v2, v234
	s_cbranch_scc1 .LBB0_347
	v_cndmask_b32_e64 v64, v64, v226, s[56:57]
	v_cndmask_b32_e64 v63, v63, v226, s[60:61]
	v_cndmask_b32_e64 v62, v62, v226, s[62:63]
	v_cndmask_b32_e64 v61, v61, v226, s[64:65]
	v_cndmask_b32_e64 v60, v60, v226, s[66:67]
	v_cndmask_b32_e64 v59, v59, v226, s[0:1]
	v_cndmask_b32_e64 v58, v58, v226, s[40:41]
	v_cndmask_b32_e64 v57, v57, v226, s[68:69]
	v_cndmask_b32_e64 v56, v56, v226, s[70:71]
	v_cndmask_b32_e64 v55, v55, v226, s[48:49]
	v_cndmask_b32_e64 v54, v54, v226, s[74:75]
	v_cndmask_b32_e64 v53, v53, v226, s[76:77]
	v_cndmask_b32_e64 v52, v52, v226, s[78:79]
	v_cndmask_b32_e64 v51, v51, v226, s[80:81]
	v_cndmask_b32_e64 v50, v50, v226, s[82:83]
	s_and_saveexec_b64 vcc, s[30:31]
	s_mov_b32 s21, 0xff800000
	v_mov_b32_e32 v65, s21
	s_or_b64 exec, exec, vcc
	v_cndmask_b32_e64 v81, v81, v226, s[58:59]
	v_cndmask_b32_e64 v80, v80, v226, s[84:85]
	v_cndmask_b32_e64 v79, v79, v226, s[2:3]
	v_cndmask_b32_e64 v78, v78, v226, s[88:89]
	v_cndmask_b32_e64 v77, v77, v226, s[90:91]
	v_cndmask_b32_e64 v76, v76, v226, s[92:93]
	v_cndmask_b32_e64 v75, v75, v226, s[94:95]
	v_cndmask_b32_e64 v74, v74, v226, s[96:97]
	v_cndmask_b32_e64 v73, v73, v226, s[4:5]
	v_cndmask_b32_e64 v72, v72, v226, s[6:7]
	v_cndmask_b32_e64 v71, v71, v226, s[8:9]
	v_cndmask_b32_e64 v70, v70, v226, s[10:11]
	v_cndmask_b32_e64 v69, v69, v226, s[12:13]
	v_cndmask_b32_e64 v68, v68, v226, s[14:15]
	v_cndmask_b32_e64 v67, v67, v226, s[16:17]
	v_cndmask_b32_e64 v66, v66, v226, s[18:19]
.LBB0_347:
	s_nop 1
	v_mfma_f32_32x32x16_bf16 v[66:81], v[114:117], v[82:85], v[66:81]
	v_mfma_f32_32x32x16_bf16 v[66:81], v[118:121], v[86:89], v[66:81]
	v_mfma_f32_32x32x16_bf16 v[66:81], v[122:125], v[90:93], v[66:81]
	v_mfma_f32_32x32x16_bf16 v[66:81], v[126:129], v[94:97], v[66:81]
	v_mfma_f32_32x32x16_bf16 v[50:65], v[110:113], v[82:85], v[50:65]
	s_and_b64 vcc, exec, s[46:47]
	s_cbranch_vccnz .Lfx_nodmaA
	s_mov_b32 s100, s44
	s_ashr_i32 s101, s44, 31
	s_lshl_b64 s[100:101], s[100:101], 17
	s_add_u32 s100, s100, 0x200
	s_addc_u32 s101, s101, 0
	v_lshl_add_u64 v[118:119], v[144:145], 0, s[100:101]
	s_and_b32 s22, s39, 0x6000
	s_add_i32 s23, s22, s27
	s_mov_b32 m0, s23
	s_add_i32 s22, s22, s33
	global_load_lds_dwordx4 v[118:119], off
	v_lshl_add_u64 v[118:119], v[154:155], 0, s[100:101]
	s_mov_b32 m0, s22
	s_nop 0
	global_load_lds_dwordx4 v[118:119], off
	s_nop 1
	s_branch .Lfx_go

; __device__ __forceinline__ unsigned cvtpk(float lo, float hi) { f32x2_t v = {lo, hi}; bf16x2_t b = __builtin_convertvector(v, bf16x2_t); return __builtin_bit_cast(unsigned, b); }
; template <class BIAS>
; __device__ __forceinline__ void attn_tiles(char* shm, const UnitIO& io, int t_begin, int t_end, const BIAS& B, int tid) {
;     ...
;             for (int d0 = 0; d0 < 4; ++d0) { c0 = __builtin_amdgcn_mfma_f32_32x32x16_bf16(kf[2 * d0], qr[d0], c0, 0, 0, 0); c1 = __builtin_amdgcn_mfma_f32_32x32x16_bf16(kf[2 * d0 + 1], qr[d0], c1, 0, 0, 0); }
;             float s0 = 0.f;
; #pragma unroll
;             for (int r = 0; r < 16; ++r) c0[r] = __builtin_amdgcn_exp2f(c0[r]);
;             { f32x2_t s2 = (f32x2_t){c0[0], c0[1]};
; #pragma unroll
;               for (int i = 1; i < 8; ++i) s2 += (f32x2_t){c0[2 * i], c0[2 * i + 1]};
;               s0 = s2[0] + s2[1]; }
;             l_reg += s0;
; #pragma unroll
;             for (int i = 0; i < 4; ++i) { pw[0][i] = cvtpk(c0[2 * i], c0[2 * i + 1]); pw[1][i] = cvtpk(c0[8 + 2 * i], c0[9 + 2 * i]); }
;             c1x = c1;
.Lfx_go:
	v_exp_f32_e32 v66, v66
	v_exp_f32_e32 v67, v67
	v_exp_f32_e32 v68, v68
	v_exp_f32_e32 v69, v69
	v_mfma_f32_32x32x16_bf16 v[50:65], v[106:109], v[86:89], v[50:65]
	v_exp_f32_e32 v114, v70
	v_exp_f32_e32 v115, v71
	v_exp_f32_e32 v116, v72
	v_exp_f32_e32 v117, v73
	v_mfma_f32_32x32x16_bf16 v[50:65], v[102:105], v[90:93], v[50:65]
	v_exp_f32_e32 v70, v74
	v_exp_f32_e32 v71, v75
	v_exp_f32_e32 v72, v76
	v_exp_f32_e32 v73, v77
	v_mfma_f32_32x32x16_bf16 v[50:65], v[98:101], v[94:97], v[50:65]
	v_exp_f32_e32 v74, v78
	v_exp_f32_e32 v75, v79
	v_add_f32_e32 v78, v66, v68
	v_add_f32_e32 v79, v67, v69
	v_add_f32_e64 v78, v114, v78
	v_add_f32_e64 v79, v115, v79
	v_exp_f32_e32 v76, v80
	v_exp_f32_e32 v77, v81
	v_add_f32_e32 v78, v116, v78
	v_add_f32_e32 v79, v117, v79
	v_cvt_pk_bf16_f32 v66, v66, v67
	v_add_f32_e32 v78, v70, v78
	v_add_f32_e32 v79, v71, v79
	v_cvt_pk_bf16_f32 v70, v70, v71
	v_add_f32_e32 v78, v72, v78
	v_add_f32_e32 v79, v73, v79
	v_cvt_pk_bf16_f32 v67, v68, v69
	v_add_f32_e32 v78, v74, v78
	v_add_f32_e32 v79, v75, v79
	v_cvt_pk_bf16_f32 v71, v72, v73
	v_add_f32_e32 v78, v76, v78
	v_add_f32_e32 v79, v77, v79
	v_cvt_pk_bf16_f32 v68, v114, v115
	v_add_f32_e32 v78, v78, v79
	v_cvt_pk_bf16_f32 v72, v74, v75
	v_cvt_pk_bf16_f32 v69, v116, v117
	v_cvt_pk_bf16_f32 v73, v76, v77
	v_add_f32_e32 v135, v135, v78
	s_and_b64 vcc, exec, s[34:35]
	s_cbranch_vccz .LBB0_355

; #define ATT_SBAR() __builtin_amdgcn_sched_barrier(0)
; #define ATT_DMA(t, slot) do { glds16(ksrc + (long)(t) * tstep, (unsigned)__builtin_amdgcn_readfirstlane(kdst + (slot))); glds16(vsrc + (long)(t) * tstep, (unsigned)__builtin_amdgcn_readfirstlane(vdst + (slot))); } while (0)
; template <class BIAS>
; __device__ __forceinline__ void attn_tiles(char* shm, const UnitIO& io, int t_begin, int t_end, const BIAS& B, int tid) {
;     ...
;         if (rem > 3) ATT_DMA(t + 3, ((t + 3 - t_begin) & 3) * SLOTB);
;         u32x4 pw[4]; f32x16 c1x;
;         if (act) {
;             bf16x8 kf[8]; const lds_cptr kp = kp0 + sl_c;
; #pragma unroll
;             for (int j = 0; j < 4; ++j) { kf[2 * j] = *(const __attribute__((address_space(3))) bf16x8*)(kp + j * 2048); kf[2 * j + 1] = *(const __attribute__((address_space(3))) bf16x8*)(kp + j * 2048 + 512); }
;             ATT_SBAR();
;             f32x16 c0, c1; B.init(c0, c1, t);
;             ATT_SBAR();
;             asm volatile("" : "+v"(kf[0]), "+v"(kf[1]), "+v"(kf[2]), "+v"(kf[3]), "+v"(kf[4]), "+v"(kf[5]), "+v"(kf[6]), "+v"(kf[7]));
; #pragma unroll
;             for (int d0 = 0; d0 < 4; ++d0) { c0 = __builtin_amdgcn_mfma_f32_32x32x16_bf16(kf[2 * d0], qr[d0], c0, 0, 0, 0); c1 = __builtin_amdgcn_mfma_f32_32x32x16_bf16(kf[2 * d0 + 1], qr[d0], c1, 0, 0, 0); }
.Ldil_h1_go:
	s_waitcnt lgkmcnt(0)
	s_nop 0
	v_mfma_f32_32x32x16_bf16 v[82:97], v[130:133], v[98:101], v[82:97]
	v_mfma_f32_32x32x16_bf16 v[82:97], v[134:137], v[102:105], v[82:97]
	v_mfma_f32_32x32x16_bf16 v[82:97], v[138:141], v[106:109], v[82:97]
	v_mfma_f32_32x32x16_bf16 v[82:97], v[142:145], v[110:113], v[82:97]
	v_mfma_f32_32x32x16_bf16 v[34:49], v[126:129], v[98:101], v[34:49]
	s_and_b64 vcc, exec, s[68:69]
	s_cbranch_vccnz .Ldl_nodmaA
	s_add_u32 s100, s88, 3
	s_addc_u32 s101, s89, 0
	s_lshl_b64 s[100:101], s[100:101], s80
	s_lshl_b64 s[100:101], s[100:101], 1
	s_add_u32 s100, s100, 0x500
	s_addc_u32 s101, s101, 0
	v_lshl_add_u64 v[58:59], v[172:173], 0, s[100:101]
	s_and_b32 s70, s81, 0x6000
	s_add_i32 s71, s70, s78
	s_mov_b32 m0, s71
	s_add_i32 s70, s70, s79
	global_load_lds_dwordx4 v[58:59], off
	v_lshl_add_u64 v[58:59], v[174:175], 0, s[100:101]
	s_mov_b32 m0, s70
	s_nop 0
	global_load_lds_dwordx4 v[58:59], off
	s_nop 1
	s_branch .Ldl_go

; __device__ __forceinline__ unsigned cvtpk(float lo, float hi) { f32x2_t v = {lo, hi}; bf16x2_t b = __builtin_convertvector(v, bf16x2_t); return __builtin_bit_cast(unsigned, b); }
; template <class BIAS>
; __device__ __forceinline__ void attn_tiles(char* shm, const UnitIO& io, int t_begin, int t_end, const BIAS& B, int tid) {
;     ...
;             for (int d0 = 0; d0 < 4; ++d0) { c0 = __builtin_amdgcn_mfma_f32_32x32x16_bf16(kf[2 * d0], qr[d0], c0, 0, 0, 0); c1 = __builtin_amdgcn_mfma_f32_32x32x16_bf16(kf[2 * d0 + 1], qr[d0], c1, 0, 0, 0); }
;             float s0 = 0.f;
; #pragma unroll
;             for (int r = 0; r < 16; ++r) c0[r] = __builtin_amdgcn_exp2f(c0[r]);
;             { f32x2_t s2 = (f32x2_t){c0[0], c0[1]};
; #pragma unroll
;               for (int i = 1; i < 8; ++i) s2 += (f32x2_t){c0[2 * i], c0[2 * i + 1]};
;               s0 = s2[0] + s2[1]; }
;             l_reg += s0;
; #pragma unroll
;             for (int i = 0; i < 4; ++i) { pw[0][i] = cvtpk(c0[2 * i], c0[2 * i + 1]); pw[1][i] = cvtpk(c0[8 + 2 * i], c0[9 + 2 * i]); }
;             c1x = c1;
.Ldl_go:
	v_exp_f32_e32 v50, v82
	v_exp_f32_e32 v51, v83
	v_exp_f32_e32 v52, v84
	v_exp_f32_e32 v53, v85
	v_mfma_f32_32x32x16_bf16 v[34:49], v[122:125], v[102:105], v[34:49]
	v_exp_f32_e32 v56, v86
	v_exp_f32_e32 v57, v87
	v_exp_f32_e32 v58, v88
	v_exp_f32_e32 v59, v89
	v_mfma_f32_32x32x16_bf16 v[34:49], v[118:121], v[106:109], v[34:49]
	v_exp_f32_e32 v54, v90
	v_exp_f32_e32 v55, v91
	v_exp_f32_e32 v60, v92
	v_exp_f32_e32 v61, v93
	v_mfma_f32_32x32x16_bf16 v[34:49], v[114:117], v[110:113], v[34:49]
	v_add_f32_e32 v66, v50, v52
	v_add_f32_e32 v67, v51, v53
	v_exp_f32_e32 v62, v94
	v_exp_f32_e32 v63, v95
	v_add_f32_e32 v66, v56, v66
	v_add_f32_e32 v67, v57, v67
	v_exp_f32_e32 v64, v96
	v_exp_f32_e32 v65, v97
	v_add_f32_e32 v66, v58, v66
	v_add_f32_e32 v67, v59, v67
	v_cvt_pk_bf16_f32 v50, v50, v51
	v_add_f32_e32 v66, v54, v66
	v_add_f32_e32 v67, v55, v67
	v_cvt_pk_bf16_f32 v54, v54, v55
	v_add_f32_e32 v66, v60, v66
	v_add_f32_e32 v67, v61, v67
	v_cvt_pk_bf16_f32 v51, v52, v53
	v_add_f32_e32 v66, v62, v66
	v_add_f32_e32 v67, v63, v67
	v_cvt_pk_bf16_f32 v55, v60, v61
	v_add_f32_e32 v66, v64, v66
	v_add_f32_e32 v67, v65, v67
	v_cvt_pk_bf16_f32 v52, v56, v57
	v_add_f32_e32 v66, v66, v67
	v_cvt_pk_bf16_f32 v56, v62, v63
	v_cvt_pk_bf16_f32 v53, v58, v59
	v_cvt_pk_bf16_f32 v57, v64, v65
	v_add_f32_e32 v151, v151, v66
	s_and_b64 vcc, exec, s[56:57]
	s_cbranch_vccz .LBB0_375
